# router loop: gamma loads for chunks 2-4 issued early into spare VGPRs, counted vmcnt keeps x and weight prefetches in flight
# baseline (speedup 1.0000x reference)
; __device__ __forceinline__ unsigned cvt_pk_bf16(float lo, float hi) { unsigned r; asm volatile("v_cvt_pk_bf16_f32 %0, %1, %2" : "=v"(r) : "v"(lo), "v"(hi)); return r; }
; __device__ __forceinline__ void p7_ffn_prep(const Ctx& C, bool dummy = false) {
;     ...
;         for (int c4 = 0; c4 < 64; c4 += 4) {
; #pragma unroll
;           for (int d = 0; d < 4; ++d) { const int cl = c4 + d, c = P7_RC(cl);
;             const f32x8 xf = __builtin_convertvector(xq[d], f32x8); const f32x4 xa = {xf[0], xf[1], xf[2], xf[3]}, xb = {xf[4], xf[5], xf[6], xf[7]}, ga = *(const f32x4*)(fg + 32 * c), gb = *(const f32x4*)(fg + 32 * c + 4);
;             const bf16x8 b0h = b0hN, b1h = b1hN, b0l = b0lN, b1l = b1lN;
;             { const int cx = P7_RC(cl + 4 < 64 ? cl + 4 : 63); xq[d] = *(const f16x8*)(x1 + 32 * cx);
;               const int cn = P7_RC(cl < 63 ? cl + 1 : cl); const size_t bn = (size_t)i * D_ + 32 * cn + 8 * g4;
;               b0hN = *(const bf16x8*)(WRH + bn); b1hN = *(const bf16x8*)(WRH + bn + (size_t)16 * D_); b0lN = *(const bf16x8*)(WRL + bn); b1lN = *(const bf16x8*)(WRL + bn + (size_t)16 * D_); }
;             float h[8]; h[0] = xa[0] * ga[0] * rstd; h[1] = xa[1] * ga[1] * rstd; h[2] = xa[2] * ga[2] * rstd; h[3] = xa[3] * ga[3] * rstd; h[4] = xb[0] * gb[0] * rstd; h[5] = xb[1] * gb[1] * rstd; h[6] = xb[2] * gb[2] * rstd; h[7] = xb[3] * gb[3] * rstd;
;             u32x4 hi; hi.x = cvt_pk_bf16(h[0], h[1]); hi.y = cvt_pk_bf16(h[2], h[3]); hi.z = cvt_pk_bf16(h[4], h[5]); hi.w = cvt_pk_bf16(h[6], h[7]);
;             { u32x2 w8; w8.x = pk4_fp8(h[0], h[1], h[2], h[3]); w8.y = pk4_fp8(h[4], h[5], h[6], h[7]); *(u32x2*)(h2 + 32 * c) = w8; }
.LBB0_899:
	s_add_i32 s0, s7, 0xffffffa0
	s_sub_i32 s3, s7, 64
	s_add_i32 s4, s6, -2
	s_add_i32 s10, s6, -1
	s_min_u32 s12, s6, 59
	s_and_b32 s90, s0, 0x7e0
	s_mov_b32 s13, s91
	s_and_b32 s14, s3, 0x7e0
	s_min_u32 s3, s4, 59
	s_min_u32 s4, s10, 59
	s_add_i32 s10, s12, s85
	s_lshl_b32 s12, s90, 2
	s_waitcnt vmcnt(5)
	v_cvt_f32_f16_sdwa v138, v27 dst_sel:DWORD dst_unused:UNUSED_PAD src0_sel:WORD_1
	v_cvt_f32_f16_sdwa v139, v26 dst_sel:DWORD dst_unused:UNUSED_PAD src0_sel:WORD_1
	v_cvt_f32_f16_e32 v142, v27
	v_cvt_f32_f16_e32 v143, v26
	s_waitcnt vmcnt(5)
	v_cvt_f32_f16_sdwa v147, v18 dst_sel:DWORD dst_unused:UNUSED_PAD src0_sel:WORD_1
	v_cvt_f32_f16_e32 v151, v18
	v_or_b32_e32 v18, s14, v77
	v_lshl_add_u64 v[26:27], v[66:67], 0, s[12:13]
	v_cvt_f32_f16_sdwa v136, v29 dst_sel:DWORD dst_unused:UNUSED_PAD src0_sel:WORD_1
	v_cvt_f32_f16_sdwa v137, v28 dst_sel:DWORD dst_unused:UNUSED_PAD src0_sel:WORD_1
	v_cvt_f32_f16_e32 v140, v29
	v_cvt_f32_f16_e32 v141, v28
	v_cvt_f32_f16_sdwa v144, v21 dst_sel:DWORD dst_unused:UNUSED_PAD src0_sel:WORD_1
	v_cvt_f32_f16_sdwa v145, v20 dst_sel:DWORD dst_unused:UNUSED_PAD src0_sel:WORD_1
	v_cvt_f32_f16_sdwa v146, v19 dst_sel:DWORD dst_unused:UNUSED_PAD src0_sel:WORD_1
	v_cvt_f32_f16_e32 v148, v21
	v_cvt_f32_f16_e32 v149, v20
	v_cvt_f32_f16_e32 v150, v19
	v_lshlrev_b32_e32 v42, 1, v18
	global_load_dwordx4 v[18:21], v[26:27], off
	s_nop 0
	global_load_dwordx4 v[26:29], v[26:27], off offset:16
	s_add_i32 s3, s3, s85
	v_cvt_f32_f16_sdwa v130, v31 dst_sel:DWORD dst_unused:UNUSED_PAD src0_sel:WORD_1
	v_cvt_f32_f16_sdwa v131, v30 dst_sel:DWORD dst_unused:UNUSED_PAD src0_sel:WORD_1
	v_cvt_f32_f16_e32 v134, v31
	v_cvt_f32_f16_e32 v135, v30
	v_lshl_add_u64 v[30:31], v[64:65], 0, s[90:91]
	s_lshl_b32 s90, s14, 2
	s_lshl_b32 s3, s3, 6
	v_cvt_f32_f16_sdwa v122, v35 dst_sel:DWORD dst_unused:UNUSED_PAD src0_sel:WORD_1
	v_cvt_f32_f16_sdwa v123, v34 dst_sel:DWORD dst_unused:UNUSED_PAD src0_sel:WORD_1
	v_cvt_f32_f16_e32 v126, v35
	v_cvt_f32_f16_e32 v127, v34
	v_cvt_f32_f16_sdwa v128, v33 dst_sel:DWORD dst_unused:UNUSED_PAD src0_sel:WORD_1
	v_cvt_f32_f16_sdwa v129, v32 dst_sel:DWORD dst_unused:UNUSED_PAD src0_sel:WORD_1
	v_cvt_f32_f16_e32 v132, v33
	v_cvt_f32_f16_e32 v133, v32
	s_sub_i32 s9, s7, 32
	v_lshl_add_u64 v[32:33], v[66:67], 0, s[90:91]
	v_lshl_add_u64 v[34:35], s[86:87], 0, v[42:43]
	s_and_b32 s90, s3, 0xfc0
	v_add_co_u32_e32 v94, vcc, s33, v34
	v_lshl_add_u64 v[100:101], v[62:63], 0, s[90:91]
	s_and_b32 s90, s9, 0x7e0
	v_cvt_f32_f16_sdwa v106, v37 dst_sel:DWORD dst_unused:UNUSED_PAD src0_sel:WORD_1
	v_cvt_f32_f16_sdwa v107, v36 dst_sel:DWORD dst_unused:UNUSED_PAD src0_sel:WORD_1
	v_cvt_f32_f16_e32 v124, v37
	v_cvt_f32_f16_e32 v125, v36
	global_load_dwordx4 v[84:87], v42, s[86:87]
	global_load_dwordx4 v[88:91], v42, s[88:89]
	v_lshl_add_u64 v[36:37], s[88:89], 0, v[42:43]
	v_addc_co_u32_e32 v95, vcc, 0, v35, vcc
	v_or_b32_e32 v42, s90, v77
	v_add_co_u32_e32 v96, vcc, s33, v36
	v_lshlrev_b32_e32 v42, 1, v42
	s_add_i32 s8, s6, -3
	v_addc_co_u32_e32 v97, vcc, 0, v37, vcc
	v_lshl_add_u64 v[102:103], s[86:87], 0, v[42:43]
	s_min_u32 s0, s8, 59
	v_add_co_u32_e32 v102, vcc, s33, v102
	s_add_i32 s0, s0, s85
	v_lshl_add_u64 v[104:105], s[88:89], 0, v[42:43]
	v_addc_co_u32_e32 v103, vcc, 0, v103, vcc
	s_mov_b32 s15, s91
	s_lshl_b32 s0, s0, 6
	v_add_co_u32_e32 v120, vcc, s33, v104
	s_mov_b32 s11, s91
	v_lshl_add_u64 v[108:109], v[64:65], 0, s[14:15]
	s_lshl_b32 s14, s10, 6
	s_and_b32 s10, s0, 0xfc0
	v_addc_co_u32_e32 v121, vcc, 0, v105, vcc
	v_lshl_add_u64 v[92:93], v[62:63], 0, s[10:11]
	v_mov_b32_e32 v68, v43
	v_mov_b32_e32 v69, v43
	global_load_dwordx4 v[34:37], v[92:93], off
	s_nop 0
	global_load_dwordx4 v[92:95], v[94:95], off
	s_nop 0
	global_load_dwordx4 v[96:99], v[96:97], off
	s_and_b32 s2, s7, 0x7e0
	v_or_b32_e32 v152, s2, v77
	v_mov_b32_e32 v70, v43
	v_mov_b32_e32 v71, v43
	s_add_i32 s4, s4, s85
	s_mov_b32 s1, s91
	s_lshl_b32 s4, s4, 6
	s_lshl_b32 s0, s90, 2
	s_mov_b32 s5, s91
	s_and_b32 s4, s4, 0xfc0
	v_lshl_add_u64 v[114:115], v[66:67], 0, s[0:1]
	v_lshl_add_u64 v[110:111], v[62:63], 0, s[4:5]
	v_mov_b32_e32 v72, v43
	v_mov_b32_e32 v73, v43
	v_lshl_add_u64 v[112:113], v[64:65], 0, s[90:91]
	s_lshl_b32 s90, s2, 2
	v_lshl_add_u64 v[196:197], v[66:67], 0, s[90:91]
	global_load_dwordx4 v[172:175], v[32:33], off
	global_load_dwordx4 v[176:179], v[32:33], off offset:16
	global_load_dwordx4 v[180:183], v[114:115], off
	global_load_dwordx4 v[184:187], v[114:115], off offset:16
	global_load_dwordx4 v[188:191], v[196:197], off
	global_load_dwordx4 v[192:195], v[196:197], off offset:16
	s_waitcnt vmcnt(11) lgkmcnt(0)
; __device__ __forceinline__ void p7_ffn_prep(const Ctx& C, bool dummy = false) {
;     ...
;           for (int d = 0; d < 4; ++d) { const int cl = c4 + d, c = P7_RC(cl);
;             const f32x8 xf = __builtin_convertvector(xq[d], f32x8); const f32x4 xa = {xf[0], xf[1], xf[2], xf[3]}, xb = {xf[4], xf[5], xf[6], xf[7]}, ga = *(const f32x4*)(fg + 32 * c), gb = *(const f32x4*)(fg + 32 * c + 4);
;             const bf16x8 b0h = b0hN, b1h = b1hN, b0l = b0lN, b1l = b1lN;
;             { const int cx = P7_RC(cl + 4 < 64 ? cl + 4 : 63); xq[d] = *(const f16x8*)(x1 + 32 * cx);
;               const int cn = P7_RC(cl < 63 ? cl + 1 : cl); const size_t bn = (size_t)i * D_ + 32 * cn + 8 * g4;
;               b0hN = *(const bf16x8*)(WRH + bn); b1hN = *(const bf16x8*)(WRH + bn + (size_t)16 * D_); b0lN = *(const bf16x8*)(WRL + bn); b1lN = *(const bf16x8*)(WRL + bn + (size_t)16 * D_); }
;             float h[8]; h[0] = xa[0] * ga[0] * rstd; h[1] = xa[1] * ga[1] * rstd; h[2] = xa[2] * ga[2] * rstd; h[3] = xa[3] * ga[3] * rstd; h[4] = xb[0] * gb[0] * rstd; h[5] = xb[1] * gb[1] * rstd; h[6] = xb[2] * gb[2] * rstd; h[7] = xb[3] * gb[3] * rstd;
;             u32x4 hi; hi.x = cvt_pk_bf16(h[0], h[1]); hi.y = cvt_pk_bf16(h[2], h[3]); hi.z = cvt_pk_bf16(h[4], h[5]); hi.w = cvt_pk_bf16(h[6], h[7]);
;             { u32x2 w8; w8.x = pk4_fp8(h[0], h[1], h[2], h[3]); w8.y = pk4_fp8(h[4], h[5], h[6], h[7]); *(u32x2*)(h2 + 32 * c) = w8; }
;             u32x4 lo; lo.x = cvt_pk_bf16(h[0] - __uint_as_float(hi.x << 16), h[1] - __uint_as_float(hi.x & 0xFFFF0000u)); lo.y = cvt_pk_bf16(h[2] - __uint_as_float(hi.y << 16), h[3] - __uint_as_float(hi.y & 0xFFFF0000u));
;             lo.z = cvt_pk_bf16(h[4] - __uint_as_float(hi.z << 16), h[5] - __uint_as_float(hi.z & 0xFFFF0000u)); lo.w = cvt_pk_bf16(h[6] - __uint_as_float(hi.w << 16), h[7] - __uint_as_float(hi.w & 0xFFFF0000u));
;             const bf16x8 ah = __builtin_bit_cast(bf16x8, hi), al = __builtin_bit_cast(bf16x8, lo);
;             a0 = __builtin_amdgcn_mfma_f32_16x16x32_bf16(ah, b0h, a0, 0, 0, 0); a0 = __builtin_amdgcn_mfma_f32_16x16x32_bf16(ah, b0l, a0, 0, 0, 0); a0 = __builtin_amdgcn_mfma_f32_16x16x32_bf16(al, b0h, a0, 0, 0, 0);
;             a1 = __builtin_amdgcn_mfma_f32_16x16x32_bf16(ah, b1h, a1, 0, 0, 0); a1 = __builtin_amdgcn_mfma_f32_16x16x32_bf16(ah, b1l, a1, 0, 0, 0); a1 = __builtin_amdgcn_mfma_f32_16x16x32_bf16(al, b1h, a1, 0, 0, 0);
	v_mul_f32_e32 v104, v18, v127
	v_mul_f32_e32 v105, v19, v123
	v_mul_f32_e32 v123, v20, v126
	v_mul_f32_e32 v122, v21, v122
	v_mul_f32_e32 v125, v125, v26
	v_mul_f32_e32 v107, v107, v27
	v_mul_f32_e32 v124, v124, v28
	v_mul_f32_e32 v106, v106, v29
	v_mul_f32_e32 v26, v83, v104
	v_mul_f32_e32 v27, v83, v105
	v_mul_f32_e32 v28, v83, v123
	v_mul_f32_e32 v29, v83, v122
	v_mul_f32_e32 v126, v83, v125
	v_mul_f32_e32 v127, v83, v107
	v_cvt_pk_bf16_f32 v18, v26, v27
	v_cvt_pk_bf16_f32 v19, v28, v29
	v_med3_f32 v26, v26, s82, v81
	v_med3_f32 v27, v27, s82, v81
	v_med3_f32 v156, v28, s82, v81
	v_med3_f32 v157, v29, s82, v81
	v_med3_f32 v28, v126, s82, v81
	v_med3_f32 v29, v127, s82, v81
	v_cvt_pk_fp8_f32 v68, v26, v27
	v_cvt_pk_fp8_f32 v69, v28, v29
	v_mul_f32_e32 v154, v83, v124
	v_mul_f32_e32 v155, v83, v106
	v_cvt_pk_bf16_f32 v20, v126, v127
	v_med3_f32 v126, v154, s82, v81
	v_med3_f32 v127, v155, s82, v81
	v_cvt_pk_bf16_f32 v21, v154, v155
	v_cvt_pk_fp8_f32 v68, v156, v157 op_sel:[0,0,1]
	v_mfma_f32_16x16x32_bf16 v[22:25], v[18:21], v[6:9], v[22:25]
	v_cvt_pk_fp8_f32 v69, v126, v127 op_sel:[0,0,1]
	v_lshlrev_b32_e32 v154, 16, v18
	v_and_b32_e32 v155, 0xffff0000, v18
	v_mfma_f32_16x16x32_bf16 v[26:29], v[18:21], v[2:5], v[38:41]
	v_lshlrev_b32_e32 v158, 16, v19
	v_and_b32_e32 v159, 0xffff0000, v19
	v_lshlrev_b32_e32 v160, 16, v20
	v_and_b32_e32 v161, 0xffff0000, v20
	v_lshlrev_b32_e32 v162, 16, v21
	v_and_b32_e32 v163, 0xffff0000, v21
	v_fma_f32 v38, v83, v104, -v154
	v_fma_f32 v39, v83, v105, -v155
	v_fma_f32 v40, v83, v123, -v158
	v_fma_f32 v41, v83, v122, -v159
	v_fma_f32 v104, v83, v125, -v160
	v_fma_f32 v105, v83, v107, -v161
	v_fma_f32 v107, v83, v124, -v162
	v_fma_f32 v106, v83, v106, -v163
	v_mfma_f32_16x16x32_bf16 v[10:13], v[18:21], v[10:13], v[22:25]
	global_store_dwordx2 v[30:31], v[68:69], off
	v_lshl_add_u64 v[116:117], v[66:67], 0, s[90:91]
	s_and_b32 s90, s14, 0xfc0
	v_mfma_f32_16x16x32_bf16 v[14:17], v[18:21], v[14:17], v[26:29]
	v_cvt_pk_bf16_f32 v18, v38, v39
	v_cvt_pk_bf16_f32 v19, v40, v41
	v_cvt_pk_bf16_f32 v20, v104, v105
	v_cvt_pk_bf16_f32 v21, v107, v106
	s_nop 0
	s_nop 1
	s_nop 0
	s_nop 0
	global_load_dwordx4 v[30:33], v[100:101], off
	global_load_dwordx4 v[38:41], v[102:103], off
	s_nop 0
	global_load_dwordx4 v[100:103], v42, s[88:89]
	v_mfma_f32_16x16x32_bf16 v[6:9], v[18:21], v[6:9], v[10:13]
	global_load_dwordx4 v[104:107], v42, s[86:87]
	s_nop 1
	global_load_dwordx4 v[10:13], v[120:121], off
	v_lshlrev_b32_e32 v42, 1, v152
	s_cmp_lt_u32 s6, 63
	v_mfma_f32_16x16x32_bf16 v[2:5], v[18:21], v[2:5], v[14:17]
	s_cselect_b64 s[0:1], -1, 0
	s_cmp_lg_u64 s[0:1], 0
	s_addc_u32 s0, s84, s6
	v_lshl_add_u64 v[14:15], s[86:87], 0, v[42:43]
	v_add_co_u32_e32 v68, vcc, s33, v14
	v_lshl_add_u64 v[16:17], s[88:89], 0, v[42:43]
	s_nop 0
	v_addc_co_u32_e32 v69, vcc, 0, v15, vcc
	v_add_co_u32_e32 v120, vcc, s33, v16
	s_lshl_b32 s0, s0, 5
	s_nop 0
	v_addc_co_u32_e32 v121, vcc, 0, v17, vcc
	s_and_b32 s0, s0, 0x7e0
	v_or_b32_e32 v153, s0, v77
	v_lshl_add_u64 v[118:119], v[62:63], 0, s[90:91]
	s_mov_b32 s3, s91
	s_add_i32 s6, s6, 4
	s_addk_i32 s7, 0x80
	s_cmp_gt_u32 s8, 59
	s_waitcnt vmcnt(10) lgkmcnt(0)
	v_mul_f32_e32 v18, v135, v172
	v_mul_f32_e32 v19, v131, v173
	v_mul_f32_e32 v22, v133, v176
	v_mul_f32_e32 v23, v129, v177
	v_mul_f32_e32 v20, v134, v174
	v_mul_f32_e32 v21, v130, v175
	v_mul_f32_e32 v26, v83, v18
	v_mul_f32_e32 v27, v83, v19
	v_mul_f32_e32 v122, v83, v22
	v_mul_f32_e32 v123, v83, v23
	v_mul_f32_e32 v24, v132, v178
	v_mul_f32_e32 v25, v128, v179
	v_mul_f32_e32 v28, v83, v20
	v_mul_f32_e32 v29, v83, v21
	v_cvt_pk_bf16_f32 v14, v26, v27
	v_cvt_pk_bf16_f32 v15, v28, v29
	v_cvt_pk_bf16_f32 v16, v122, v123
	v_med3_f32 v26, v26, s82, v81
	v_med3_f32 v27, v27, s82, v81
	v_med3_f32 v122, v122, s82, v81
	v_med3_f32 v123, v123, s82, v81
	v_cvt_pk_fp8_f32 v70, v26, v27
	v_cvt_pk_fp8_f32 v71, v122, v123
	v_mul_f32_e32 v124, v83, v24
	v_mul_f32_e32 v125, v83, v25
	v_cvt_pk_bf16_f32 v17, v124, v125
	v_med3_f32 v28, v28, s82, v81
	v_med3_f32 v29, v29, s82, v81
	v_med3_f32 v124, v124, s82, v81
	v_med3_f32 v125, v125, s82, v81
	v_mfma_f32_16x16x32_bf16 v[6:9], v[14:17], v[84:87], v[6:9]
	v_cvt_pk_fp8_f32 v70, v28, v29 op_sel:[0,0,1]
	v_cvt_pk_fp8_f32 v71, v124, v125 op_sel:[0,0,1]
	v_lshlrev_b32_e32 v26, 16, v14
	v_mfma_f32_16x16x32_bf16 v[2:5], v[14:17], v[92:95], v[2:5]
	v_and_b32_e32 v27, 0xffff0000, v14
	v_lshlrev_b32_e32 v122, 16, v15
	v_and_b32_e32 v123, 0xffff0000, v15
	v_lshlrev_b32_e32 v126, 16, v16
	v_and_b32_e32 v127, 0xffff0000, v16
	v_lshlrev_b32_e32 v128, 16, v17
	v_and_b32_e32 v129, 0xffff0000, v17
	v_fma_f32 v18, v83, v18, -v26
	v_fma_f32 v19, v83, v19, -v27
	v_fma_f32 v20, v83, v20, -v122
	v_fma_f32 v21, v83, v21, -v123
	v_fma_f32 v22, v83, v22, -v126
	v_fma_f32 v23, v83, v23, -v127
	v_fma_f32 v24, v83, v24, -v128
	v_fma_f32 v25, v83, v25, -v129
	v_mfma_f32_16x16x32_bf16 v[6:9], v[14:17], v[88:91], v[6:9]
	global_store_dwordx2 v[108:109], v[70:71], off
	v_mfma_f32_16x16x32_bf16 v[2:5], v[14:17], v[96:99], v[2:5]
	v_cvt_pk_bf16_f32 v14, v18, v19
	v_cvt_pk_bf16_f32 v15, v20, v21
	v_cvt_pk_bf16_f32 v16, v22, v23
	v_cvt_pk_bf16_f32 v17, v24, v25
	s_nop 0
	s_nop 0
	global_load_dwordx4 v[26:29], v[110:111], off
	s_nop 0
	global_load_dwordx4 v[68:71], v[68:69], off
	s_nop 0
	global_load_dwordx4 v[88:91], v42, s[88:89]
	v_mfma_f32_16x16x32_bf16 v[2:5], v[14:17], v[92:95], v[2:5]
	s_waitcnt vmcnt(12) lgkmcnt(0)
; __device__ __forceinline__ void p7_ffn_prep(const Ctx& C, bool dummy = false) {
;     ...
;           for (int d = 0; d < 4; ++d) { const int cl = c4 + d, c = P7_RC(cl);
;             const f32x8 xf = __builtin_convertvector(xq[d], f32x8); const f32x4 xa = {xf[0], xf[1], xf[2], xf[3]}, xb = {xf[4], xf[5], xf[6], xf[7]}, ga = *(const f32x4*)(fg + 32 * c), gb = *(const f32x4*)(fg + 32 * c + 4);
;             const bf16x8 b0h = b0hN, b1h = b1hN, b0l = b0lN, b1l = b1lN;
;             { const int cx = P7_RC(cl + 4 < 64 ? cl + 4 : 63); xq[d] = *(const f16x8*)(x1 + 32 * cx);
;               const int cn = P7_RC(cl < 63 ? cl + 1 : cl); const size_t bn = (size_t)i * D_ + 32 * cn + 8 * g4;
;               b0hN = *(const bf16x8*)(WRH + bn); b1hN = *(const bf16x8*)(WRH + bn + (size_t)16 * D_); b0lN = *(const bf16x8*)(WRL + bn); b1lN = *(const bf16x8*)(WRL + bn + (size_t)16 * D_); }
;             float h[8]; h[0] = xa[0] * ga[0] * rstd; h[1] = xa[1] * ga[1] * rstd; h[2] = xa[2] * ga[2] * rstd; h[3] = xa[3] * ga[3] * rstd; h[4] = xb[0] * gb[0] * rstd; h[5] = xb[1] * gb[1] * rstd; h[6] = xb[2] * gb[2] * rstd; h[7] = xb[3] * gb[3] * rstd;
;             u32x4 hi; hi.x = cvt_pk_bf16(h[0], h[1]); hi.y = cvt_pk_bf16(h[2], h[3]); hi.z = cvt_pk_bf16(h[4], h[5]); hi.w = cvt_pk_bf16(h[6], h[7]);
;             { u32x2 w8; w8.x = pk4_fp8(h[0], h[1], h[2], h[3]); w8.y = pk4_fp8(h[4], h[5], h[6], h[7]); *(u32x2*)(h2 + 32 * c) = w8; }
;             u32x4 lo; lo.x = cvt_pk_bf16(h[0] - __uint_as_float(hi.x << 16), h[1] - __uint_as_float(hi.x & 0xFFFF0000u)); lo.y = cvt_pk_bf16(h[2] - __uint_as_float(hi.y << 16), h[3] - __uint_as_float(hi.y & 0xFFFF0000u));
;             lo.z = cvt_pk_bf16(h[4] - __uint_as_float(hi.z << 16), h[5] - __uint_as_float(hi.z & 0xFFFF0000u)); lo.w = cvt_pk_bf16(h[6] - __uint_as_float(hi.w << 16), h[7] - __uint_as_float(hi.w & 0xFFFF0000u));
;             const bf16x8 ah = __builtin_bit_cast(bf16x8, hi), al = __builtin_bit_cast(bf16x8, lo);
;             a0 = __builtin_amdgcn_mfma_f32_16x16x32_bf16(ah, b0h, a0, 0, 0, 0); a0 = __builtin_amdgcn_mfma_f32_16x16x32_bf16(ah, b0l, a0, 0, 0, 0); a0 = __builtin_amdgcn_mfma_f32_16x16x32_bf16(al, b0h, a0, 0, 0, 0);
;             a1 = __builtin_amdgcn_mfma_f32_16x16x32_bf16(ah, b1h, a1, 0, 0, 0); a1 = __builtin_amdgcn_mfma_f32_16x16x32_bf16(ah, b1l, a1, 0, 0, 0); a1 = __builtin_amdgcn_mfma_f32_16x16x32_bf16(al, b1h, a1, 0, 0, 0);
	v_mul_f32_e32 v18, v143, v180
	v_mul_f32_e32 v19, v139, v181
	v_mul_f32_e32 v22, v141, v184
	v_mul_f32_e32 v23, v137, v185
	v_mul_f32_e32 v20, v142, v182
	v_mul_f32_e32 v21, v138, v183
	v_mul_f32_e32 v92, v83, v18
	v_mul_f32_e32 v93, v83, v19
	v_mul_f32_e32 v108, v83, v22
	v_mul_f32_e32 v109, v83, v23
	v_mfma_f32_16x16x32_bf16 v[6:9], v[14:17], v[84:87], v[6:9]
	global_load_dwordx4 v[84:87], v42, s[86:87]
	global_load_dwordx4 v[96:99], v[120:121], off
	v_mul_f32_e32 v94, v83, v20
	v_mul_f32_e32 v95, v83, v21
	v_cvt_pk_bf16_f32 v14, v92, v93
	v_cvt_pk_bf16_f32 v15, v94, v95
	v_cvt_pk_bf16_f32 v16, v108, v109
	v_med3_f32 v92, v92, s82, v81
	v_med3_f32 v93, v93, s82, v81
	v_med3_f32 v108, v108, s82, v81
	v_med3_f32 v109, v109, s82, v81
	v_cvt_pk_fp8_f32 v72, v92, v93
	v_cvt_pk_fp8_f32 v73, v108, v109
	v_mul_f32_e32 v24, v140, v186
	v_mul_f32_e32 v25, v136, v187
	v_mul_f32_e32 v110, v83, v24
	v_mul_f32_e32 v111, v83, v25
	v_cvt_pk_bf16_f32 v17, v110, v111
	v_med3_f32 v94, v94, s82, v81
	v_med3_f32 v95, v95, s82, v81
	v_med3_f32 v110, v110, s82, v81
	v_med3_f32 v111, v111, s82, v81
	v_cvt_pk_fp8_f32 v72, v94, v95 op_sel:[0,0,1]
	v_cvt_pk_fp8_f32 v73, v110, v111 op_sel:[0,0,1]
	v_lshlrev_b32_e32 v92, 16, v14
	v_and_b32_e32 v93, 0xffff0000, v14
	v_lshlrev_b32_e32 v108, 16, v15
	v_lshlrev_b32_e32 v122, 16, v16
	v_and_b32_e32 v123, 0xffff0000, v16
	v_lshlrev_b32_e32 v124, 16, v17
	v_and_b32_e32 v125, 0xffff0000, v17
	v_and_b32_e32 v109, 0xffff0000, v15
	v_fma_f32 v18, v83, v18, -v92
	v_fma_f32 v19, v83, v19, -v93
	v_fma_f32 v20, v83, v20, -v108
	v_fma_f32 v92, v83, v22, -v122
	v_fma_f32 v93, v83, v23, -v123
	v_fma_f32 v108, v83, v24, -v124
	v_fma_f32 v25, v83, v25, -v125
	v_fma_f32 v21, v83, v21, -v109
	global_store_dwordx2 v[112:113], v[72:73], off
	v_cvt_pk_bf16_f32 v22, v18, v19
	v_cvt_pk_bf16_f32 v23, v20, v21
	v_cvt_pk_bf16_f32 v24, v92, v93
	v_cvt_pk_bf16_f32 v25, v108, v25
	s_nop 0
	s_nop 0
	v_lshlrev_b32_e32 v42, 1, v153
	v_lshl_add_u64 v[114:115], s[86:87], 0, v[42:43]
	s_waitcnt vmcnt(8)
	v_mfma_f32_16x16x32_bf16 v[6:9], v[14:17], v[104:107], v[6:9]
	v_add_co_u32_e32 v72, vcc, s33, v114
	v_lshl_add_u64 v[120:121], s[88:89], 0, v[42:43]
	v_mfma_f32_16x16x32_bf16 v[2:5], v[14:17], v[38:41], v[2:5]
	v_addc_co_u32_e32 v73, vcc, 0, v115, vcc
	v_add_co_u32_e32 v116, vcc, s33, v120
	v_mfma_f32_16x16x32_bf16 v[100:103], v[14:17], v[100:103], v[6:9]
	s_nop 0
	v_addc_co_u32_e32 v117, vcc, 0, v121, vcc
	s_waitcnt vmcnt(7) lgkmcnt(0)
	v_mul_f32_e32 v108, v149, v192
	v_mfma_f32_16x16x32_bf16 v[112:115], v[14:17], v[10:13], v[2:5]
	global_load_dwordx4 v[18:21], v[118:119], off
	s_nop 1
	global_load_dwordx4 v[2:5], v[72:73], off
	global_load_dwordx4 v[10:13], v42, s[88:89]
	global_load_dwordx4 v[6:9], v42, s[86:87]
	global_load_dwordx4 v[14:17], v[116:117], off
	v_mul_f32_e32 v42, v151, v188
	v_mul_f32_e32 v109, v145, v193
	v_mfma_f32_16x16x32_bf16 v[100:103], v[22:25], v[104:107], v[100:103]
	v_mul_f32_e32 v106, v147, v189
	v_mul_f32_e32 v107, v150, v190
	v_mul_f32_e32 v92, v83, v42
	v_mfma_f32_16x16x32_bf16 v[22:25], v[22:25], v[38:41], v[112:115]
	v_mul_f32_e32 v93, v83, v106
	v_mul_f32_e32 v94, v83, v107
	v_mov_b32_e32 v72, v43
	v_mul_f32_e32 v112, v146, v191
	v_mul_f32_e32 v95, v83, v112
	v_mul_f32_e32 v113, v83, v108
	v_mul_f32_e32 v114, v83, v109
	v_mov_b32_e32 v73, v43
	v_mul_f32_e32 v110, v148, v194
	v_mul_f32_e32 v111, v144, v195
	v_cvt_pk_bf16_f32 v38, v92, v93
	v_cvt_pk_bf16_f32 v39, v94, v95
	v_med3_f32 v92, v92, s82, v81
	v_med3_f32 v93, v93, s82, v81
	v_med3_f32 v117, v94, s82, v81
	v_med3_f32 v118, v95, s82, v81
	v_med3_f32 v94, v113, s82, v81
	v_med3_f32 v95, v114, s82, v81
	v_mul_f32_e32 v115, v83, v110
	v_mul_f32_e32 v116, v83, v111
	v_cvt_pk_bf16_f32 v40, v113, v114
	v_cvt_pk_bf16_f32 v41, v115, v116
	v_cvt_pk_fp8_f32 v72, v92, v93
	v_cvt_pk_fp8_f32 v73, v94, v95
	s_waitcnt vmcnt(6)
	v_mfma_f32_16x16x32_bf16 v[92:95], v[38:41], v[84:87], v[100:103]
	v_med3_f32 v113, v115, s82, v81
	v_med3_f32 v114, v116, s82, v81
	v_lshlrev_b32_e32 v115, 16, v38
	v_mfma_f32_16x16x32_bf16 v[22:25], v[38:41], v[68:71], v[22:25]
	v_and_b32_e32 v116, 0xffff0000, v38
	v_lshlrev_b32_e32 v119, 16, v39
	v_and_b32_e32 v120, 0xffff0000, v39
	v_lshlrev_b32_e32 v121, 16, v40
	v_and_b32_e32 v100, 0xffff0000, v40
	v_lshlrev_b32_e32 v101, 16, v41
	v_and_b32_e32 v102, 0xffff0000, v41
	v_cvt_pk_fp8_f32 v72, v117, v118 op_sel:[0,0,1]
	v_mfma_f32_16x16x32_bf16 v[88:91], v[38:41], v[88:91], v[92:95]
	v_cvt_pk_fp8_f32 v73, v113, v114 op_sel:[0,0,1]
	v_lshl_add_u64 v[104:105], v[64:65], 0, s[2:3]
	v_fma_f32 v42, v83, v42, -v115
	v_mfma_f32_16x16x32_bf16 v[38:41], v[38:41], v[96:99], v[22:25]
	v_fma_f32 v103, v83, v106, -v116
	v_fma_f32 v106, v83, v107, -v119
	v_fma_f32 v107, v83, v112, -v120
	v_fma_f32 v108, v83, v108, -v121
	v_fma_f32 v100, v83, v109, -v100
	v_fma_f32 v101, v83, v110, -v101
	v_fma_f32 v102, v83, v111, -v102
	global_store_dwordx2 v[104:105], v[72:73], off
	v_cvt_pk_bf16_f32 v92, v42, v103
	v_cvt_pk_bf16_f32 v93, v106, v107
	v_cvt_pk_bf16_f32 v94, v108, v100
	v_cvt_pk_bf16_f32 v95, v101, v102
	s_nop 0
	v_mfma_f32_16x16x32_bf16 v[22:25], v[92:95], v[84:87], v[88:91]
	v_mfma_f32_16x16x32_bf16 v[38:41], v[92:95], v[68:71], v[38:41]
	s_cbranch_scc0 .LBB0_899
	s_waitcnt vmcnt(4)
	v_add_u32_e32 v2, 0x400, v74
	s_nop 4
	ds_write2_b32 v2, v22, v38 offset1:16
	ds_write2_b32 v2, v23, v39 offset0:33 offset1:49
	ds_write2_b32 v2, v24, v40 offset0:66 offset1:82
	ds_write2_b32 v2, v25, v41 offset0:99 offset1:115
	s_waitcnt vmcnt(3)
	v_mov_b32_e32 v12, 0
	v_mov_b32_e32 v20, 0
	v_mov_b32_e32 v18, 0
	s_waitcnt vmcnt(1)
	v_mov_b32_e32 v16, 0
	v_mov_b32_e32 v14, 0
	v_mov_b32_e32 v10, 0
	v_mov_b32_e32 v11, 0
	v_mov_b32_e32 v13, 0
	v_mov_b32_e32 v2, 0
	v_mov_b32_e32 v4, 0
	v_mov_b32_e32 v6, 0
	v_mov_b32_e32 v8, 0
	s_mov_b64 s[2:3], exec
	v_readlane_b32 s0, v254, 22
	v_readlane_b32 s1, v254, 23
	v_writelane_b32 v254, s2, 30
	s_and_b64 s[0:1], s[2:3], s[0:1]
	s_nop 0
	v_writelane_b32 v254, s3, 31
	s_mov_b64 exec, s[0:1]
	s_cbranch_execz .LBB0_902
; __device__ __forceinline__ void p7_ffn_prep(const Ctx& C, bool dummy = false) {
;     ...
;         if (lane < 16) {
;             float v[32];
; #pragma unroll
;             for (int e = 0; e < 32; ++e) v[e] = lg[lane * 33 + e] + C.ka->in[I_BR][e];
;             float tv[4];
; #pragma unroll
;             for (int k = 0; k < 4; ++k) { float best = -__builtin_inff(); int be = 0;
; #pragma unroll
;                 for (int e = 0; e < 32; ++e) { const bool taken = (k > 0 && e == e4[0]) || (k > 1 && e == e4[1]) || (k > 2 && e == e4[2]); if (!taken && v[e] > best) { best = v[e]; be = e; } }
	v_readlane_b32 s0, v254, 15
	v_readlane_b32 s1, v254, 16
	v_add_u32_e32 v4, 0x400, v79
	ds_read2_b32 v[8:9], v4 offset1:1
	v_mov_b64_e32 v[2:3], s[0:1]
	flat_load_dwordx2 v[2:3], v[2:3] offset:176
	s_mov_b32 s0, 0xff800000
	s_waitcnt vmcnt(0) lgkmcnt(0)
	flat_load_dwordx4 v[4:7], v[2:3]
	flat_load_dwordx4 v[16:19], v[2:3] offset:16
	flat_load_dwordx4 v[20:23], v[2:3] offset:32
	flat_load_dwordx4 v[24:27], v[2:3] offset:48
	flat_load_dwordx4 v[28:31], v[2:3] offset:64
	flat_load_dwordx4 v[32:35], v[2:3] offset:80
	s_waitcnt vmcnt(0) lgkmcnt(0)
	v_add_f32_e32 v11, v8, v4
	v_add_u32_e32 v4, 0x408, v79
	v_add_f32_e32 v9, v9, v5
	ds_read2_b32 v[4:5], v4 offset1:1
	v_cmp_lg_f32_e32 vcc, s0, v11
	v_cmp_nlg_f32_e64 s[10:11], s0, v11
	s_waitcnt lgkmcnt(0)
	v_add_f32_e32 v8, v4, v6
	v_add_u32_e32 v4, 0x410, v79
	v_add_f32_e32 v7, v5, v7
	ds_read2_b32 v[4:5], v4 offset1:1
	s_waitcnt lgkmcnt(0)
	v_add_f32_e32 v15, v4, v16
	v_add_u32_e32 v4, 0x418, v79
	v_add_f32_e32 v13, v5, v17
	ds_read2_b32 v[4:5], v4 offset1:1
	s_waitcnt lgkmcnt(0)
	v_add_f32_e32 v12, v4, v18
	v_add_u32_e32 v4, 0x420, v79
	v_add_f32_e32 v10, v5, v19
	ds_read2_b32 v[4:5], v4 offset1:1
	s_waitcnt lgkmcnt(0)
	v_add_f32_e32 v19, v4, v20
	v_add_u32_e32 v4, 0x428, v79
	v_add_f32_e32 v17, v5, v21
	ds_read2_b32 v[4:5], v4 offset1:1
	s_waitcnt lgkmcnt(0)
	v_add_f32_e32 v16, v4, v22
	v_add_u32_e32 v4, 0x430, v79
	v_add_f32_e32 v14, v5, v23
	ds_read2_b32 v[4:5], v4 offset1:1
	s_waitcnt lgkmcnt(0)
	v_add_f32_e32 v23, v4, v24
	v_add_u32_e32 v4, 0x438, v79
	v_add_f32_e32 v21, v5, v25
	ds_read2_b32 v[4:5], v4 offset1:1
	s_waitcnt lgkmcnt(0)
	v_add_f32_e32 v20, v4, v26
	v_add_u32_e32 v4, 0x440, v79
	v_add_f32_e32 v18, v5, v27
	ds_read2_b32 v[4:5], v4 offset1:1
	s_waitcnt lgkmcnt(0)
	v_add_f32_e32 v27, v4, v28
	v_add_u32_e32 v4, 0x448, v79
	v_add_f32_e32 v25, v5, v29
	ds_read2_b32 v[4:5], v4 offset1:1
	s_waitcnt lgkmcnt(0)
	v_add_f32_e32 v24, v4, v30
	v_add_u32_e32 v4, 0x450, v79
	v_add_f32_e32 v22, v5, v31
	ds_read2_b32 v[4:5], v4 offset1:1
	s_waitcnt lgkmcnt(0)
	v_add_f32_e32 v31, v4, v32
	v_add_u32_e32 v4, 0x458, v79
	v_add_f32_e32 v29, v5, v33
	ds_read2_b32 v[4:5], v4 offset1:1
	s_waitcnt lgkmcnt(0)
	v_add_f32_e32 v28, v4, v34
	v_add_f32_e32 v26, v5, v35
	flat_load_dwordx4 v[34:37], v[2:3] offset:96
	v_add_u32_e32 v4, 0x460, v79
	ds_read2_b32 v[4:5], v4 offset1:1
	s_waitcnt vmcnt(0) lgkmcnt(0)
	v_add_f32_e32 v34, v4, v34
	v_add_u32_e32 v4, 0x468, v79
	v_add_f32_e32 v33, v5, v35
	ds_read2_b32 v[4:5], v4 offset1:1
	s_waitcnt lgkmcnt(0)
	v_add_f32_e32 v32, v4, v36
	v_add_u32_e32 v4, 0x470, v79
	v_add_f32_e32 v30, v5, v37
	ds_read2_b32 v[36:37], v4 offset1:1
	flat_load_dwordx4 v[2:5], v[2:3] offset:112
	s_waitcnt vmcnt(0) lgkmcnt(0)
	v_add_f32_e32 v35, v36, v2
	v_add_u32_e32 v2, 0x478, v79
	v_add_f32_e32 v3, v37, v3
	ds_read2_b32 v[36:37], v2 offset1:1
	v_cndmask_b32_e32 v2, v82, v11, vcc
	v_cmp_gt_f32_e32 vcc, v9, v2
	s_waitcnt lgkmcnt(0)
	v_add_f32_e32 v36, v36, v4
	v_cndmask_b32_e32 v2, v2, v9, vcc
	v_cndmask_b32_e64 v4, 0, 1, vcc
	v_cmp_gt_f32_e32 vcc, v8, v2
	v_add_f32_e32 v5, v37, v5
	s_nop 0
	v_cndmask_b32_e32 v2, v2, v8, vcc
	v_cndmask_b32_e64 v4, v4, 2, vcc
	v_cmp_gt_f32_e32 vcc, v7, v2
	s_nop 1
	v_cndmask_b32_e32 v2, v2, v7, vcc
	v_cndmask_b32_e64 v4, v4, 3, vcc
	v_cmp_gt_f32_e32 vcc, v15, v2
	s_nop 1
	v_cndmask_b32_e32 v2, v2, v15, vcc
	v_cndmask_b32_e64 v4, v4, 4, vcc
	v_cmp_gt_f32_e32 vcc, v13, v2
	s_nop 1
	v_cndmask_b32_e32 v2, v2, v13, vcc
	v_cndmask_b32_e64 v4, v4, 5, vcc
	v_cmp_gt_f32_e32 vcc, v12, v2
	s_nop 1
	v_cndmask_b32_e32 v2, v2, v12, vcc
	v_cndmask_b32_e64 v4, v4, 6, vcc
	v_cmp_gt_f32_e32 vcc, v10, v2
	s_nop 1
	v_cndmask_b32_e32 v2, v2, v10, vcc
	v_cndmask_b32_e64 v4, v4, 7, vcc
	v_cmp_gt_f32_e32 vcc, v19, v2
	s_nop 1
	v_cndmask_b32_e32 v2, v2, v19, vcc
	v_cndmask_b32_e64 v4, v4, 8, vcc
	v_cmp_gt_f32_e32 vcc, v17, v2
	s_nop 1
	v_cndmask_b32_e32 v2, v2, v17, vcc
	v_cndmask_b32_e64 v4, v4, 9, vcc
	v_cmp_gt_f32_e32 vcc, v16, v2
	s_nop 1
	v_cndmask_b32_e32 v2, v2, v16, vcc
	v_cndmask_b32_e64 v4, v4, 10, vcc
	v_cmp_gt_f32_e32 vcc, v14, v2
	s_nop 1
	v_cndmask_b32_e32 v2, v2, v14, vcc
	v_cndmask_b32_e64 v4, v4, 11, vcc
	v_cmp_gt_f32_e32 vcc, v23, v2
	s_nop 1
	v_cndmask_b32_e32 v2, v2, v23, vcc
	v_cndmask_b32_e64 v4, v4, 12, vcc
	v_cmp_gt_f32_e32 vcc, v21, v2
	s_nop 1
	v_cndmask_b32_e32 v2, v2, v21, vcc
	v_cndmask_b32_e64 v4, v4, 13, vcc
	v_cmp_gt_f32_e32 vcc, v20, v2
	s_nop 1
	v_cndmask_b32_e32 v2, v2, v20, vcc
	v_cndmask_b32_e64 v4, v4, 14, vcc
	v_cmp_gt_f32_e32 vcc, v18, v2
	s_nop 1
	v_cndmask_b32_e32 v2, v2, v18, vcc
	v_cndmask_b32_e64 v4, v4, 15, vcc
	v_cmp_gt_f32_e32 vcc, v27, v2
	s_nop 1
	v_cndmask_b32_e32 v2, v2, v27, vcc
	v_cndmask_b32_e64 v4, v4, 16, vcc
	v_cmp_gt_f32_e32 vcc, v25, v2
	s_nop 1
	v_cndmask_b32_e32 v2, v2, v25, vcc
	v_cndmask_b32_e64 v4, v4, 17, vcc
	v_cmp_gt_f32_e32 vcc, v24, v2
	s_nop 1
	v_cndmask_b32_e32 v2, v2, v24, vcc
	v_cndmask_b32_e64 v4, v4, 18, vcc
	v_cmp_gt_f32_e32 vcc, v22, v2
	s_nop 1
	v_cndmask_b32_e32 v2, v2, v22, vcc
	v_cndmask_b32_e64 v4, v4, 19, vcc
	v_cmp_gt_f32_e32 vcc, v31, v2
	s_nop 1
	v_cndmask_b32_e32 v2, v2, v31, vcc
	v_cndmask_b32_e64 v4, v4, 20, vcc
	v_cmp_gt_f32_e32 vcc, v29, v2
	s_nop 1
	v_cndmask_b32_e32 v2, v2, v29, vcc
	v_cndmask_b32_e64 v4, v4, 21, vcc
	v_cmp_gt_f32_e32 vcc, v28, v2
	s_nop 1
	v_cndmask_b32_e32 v2, v2, v28, vcc
	v_cndmask_b32_e64 v4, v4, 22, vcc
	v_cmp_gt_f32_e32 vcc, v26, v2
	s_nop 1
	v_cndmask_b32_e32 v2, v2, v26, vcc
	v_cndmask_b32_e64 v4, v4, 23, vcc
	v_cmp_gt_f32_e32 vcc, v34, v2
	s_nop 1
	v_cndmask_b32_e32 v2, v2, v34, vcc
	v_cndmask_b32_e64 v4, v4, 24, vcc
	v_cmp_gt_f32_e32 vcc, v33, v2
	s_nop 1
; __device__ __forceinline__ void p7_ffn_prep(const Ctx& C, bool dummy = false) {
;     ...
;             for (int k = 0; k < 4; ++k) { float best = -__builtin_inff(); int be = 0;
; #pragma unroll
;                 for (int e = 0; e < 32; ++e) { const bool taken = (k > 0 && e == e4[0]) || (k > 1 && e == e4[1]) || (k > 2 && e == e4[2]); if (!taken && v[e] > best) { best = v[e]; be = e; } }
;                 e4[k] = be; tv[k] = best; }
	v_cndmask_b32_e32 v2, v2, v33, vcc
	v_cndmask_b32_e64 v4, v4, 25, vcc
	v_cmp_gt_f32_e32 vcc, v32, v2
	s_nop 1
	v_cndmask_b32_e32 v2, v2, v32, vcc
	v_cndmask_b32_e64 v4, v4, 26, vcc
	v_cmp_gt_f32_e32 vcc, v30, v2
	s_nop 1
	v_cndmask_b32_e32 v2, v2, v30, vcc
	v_cndmask_b32_e64 v4, v4, 27, vcc
	v_cmp_gt_f32_e32 vcc, v35, v2
	s_nop 1
	v_cndmask_b32_e32 v2, v2, v35, vcc
	v_cndmask_b32_e64 v4, v4, 28, vcc
	v_cmp_gt_f32_e32 vcc, v3, v2
	s_nop 1
	v_cndmask_b32_e32 v2, v2, v3, vcc
	v_cndmask_b32_e64 v4, v4, 29, vcc
	v_cmp_gt_f32_e32 vcc, v36, v2
	s_nop 1
	v_cndmask_b32_e32 v2, v2, v36, vcc
	v_cndmask_b32_e64 v4, v4, 30, vcc
	v_cmp_gt_f32_e32 vcc, v5, v2
	s_nop 1
	v_cndmask_b32_e32 v37, v2, v5, vcc
	v_cndmask_b32_e64 v2, v4, 31, vcc
	v_cmp_eq_u32_e32 vcc, 0, v2
	s_or_b64 vcc, vcc, s[10:11]
	v_cmp_eq_u32_e64 s[10:11], 1, v2
	v_cndmask_b32_e32 v4, v11, v82, vcc
	v_cmp_ngt_f32_e64 s[12:13], v9, v4
	s_or_b64 s[12:13], s[10:11], s[12:13]
	s_xor_b64 s[0:1], s[12:13], -1
	v_cndmask_b32_e64 v4, v9, v4, s[12:13]
	v_cndmask_b32_e64 v6, 0, 1, s[0:1]
	v_cmp_eq_u32_e64 s[0:1], 2, v2
	v_cmp_ngt_f32_e64 s[14:15], v8, v4
	s_or_b64 s[14:15], s[0:1], s[14:15]
	v_cmp_eq_u32_e64 s[2:3], 3, v2
	v_cndmask_b32_e64 v4, v8, v4, s[14:15]
	v_cmp_ngt_f32_e64 s[16:17], v7, v4
	s_or_b64 s[16:17], s[2:3], s[16:17]
	v_cndmask_b32_e64 v6, 2, v6, s[14:15]
	v_cndmask_b32_e64 v4, v7, v4, s[16:17]
	v_cndmask_b32_e64 v6, 3, v6, s[16:17]
	v_cmp_eq_u32_e64 s[16:17], 4, v2
	v_cmp_ngt_f32_e64 s[18:19], v15, v4
	s_or_b64 s[18:19], s[16:17], s[18:19]
	v_cmp_eq_u32_e64 s[72:73], 29, v2
	v_cndmask_b32_e64 v4, v15, v4, s[18:19]
	v_cndmask_b32_e64 v6, 4, v6, s[18:19]
	v_cmp_eq_u32_e64 s[18:19], 5, v2
	v_cmp_ngt_f32_e64 s[20:21], v13, v4
	s_or_b64 s[20:21], s[18:19], s[20:21]
	v_cmp_eq_u32_e64 s[70:71], 30, v2
	v_cndmask_b32_e64 v4, v13, v4, s[20:21]
	v_cndmask_b32_e64 v6, 5, v6, s[20:21]
	v_cmp_eq_u32_e64 s[20:21], 6, v2
	v_cmp_ngt_f32_e64 s[22:23], v12, v4
	s_or_b64 s[22:23], s[20:21], s[22:23]
	s_nop 0
	v_cndmask_b32_e64 v4, v12, v4, s[22:23]
	v_cndmask_b32_e64 v6, 6, v6, s[22:23]
	v_cmp_eq_u32_e64 s[22:23], 7, v2
	v_cmp_ngt_f32_e64 s[24:25], v10, v4
	s_or_b64 s[24:25], s[22:23], s[24:25]
	s_nop 0
	v_cndmask_b32_e64 v4, v10, v4, s[24:25]
	v_cndmask_b32_e64 v6, 7, v6, s[24:25]
	v_cmp_eq_u32_e64 s[24:25], 8, v2
	v_cmp_ngt_f32_e64 s[26:27], v19, v4
	s_or_b64 s[26:27], s[24:25], s[26:27]
	s_nop 0
	v_cndmask_b32_e64 v4, v19, v4, s[26:27]
	v_cndmask_b32_e64 v6, 8, v6, s[26:27]
	v_cmp_eq_u32_e64 s[26:27], 9, v2
	v_cmp_ngt_f32_e64 s[28:29], v17, v4
	s_or_b64 s[28:29], s[26:27], s[28:29]
	s_nop 0
	v_cndmask_b32_e64 v4, v17, v4, s[28:29]
	v_cndmask_b32_e64 v6, 9, v6, s[28:29]
	v_cmp_eq_u32_e64 s[28:29], 10, v2
	v_cmp_ngt_f32_e64 s[30:31], v16, v4
	s_or_b64 s[30:31], s[28:29], s[30:31]
	s_nop 0
	v_cndmask_b32_e64 v4, v16, v4, s[30:31]
	v_cndmask_b32_e64 v6, 10, v6, s[30:31]
	v_cmp_eq_u32_e64 s[30:31], 11, v2
	v_cmp_ngt_f32_e64 s[34:35], v14, v4
	s_or_b64 s[34:35], s[30:31], s[34:35]
	s_nop 0
	v_cndmask_b32_e64 v4, v14, v4, s[34:35]
	v_cndmask_b32_e64 v6, 11, v6, s[34:35]
	v_cmp_eq_u32_e64 s[34:35], 12, v2
	v_cmp_ngt_f32_e64 s[36:37], v23, v4
	s_or_b64 s[36:37], s[34:35], s[36:37]
	s_nop 0
	v_cndmask_b32_e64 v4, v23, v4, s[36:37]
	v_cndmask_b32_e64 v6, 12, v6, s[36:37]
	v_cmp_eq_u32_e64 s[36:37], 13, v2
	v_cmp_ngt_f32_e64 s[38:39], v21, v4
	s_or_b64 s[38:39], s[36:37], s[38:39]
	s_nop 0
	v_cndmask_b32_e64 v4, v21, v4, s[38:39]
	v_cndmask_b32_e64 v6, 13, v6, s[38:39]
	v_cmp_eq_u32_e64 s[38:39], 14, v2
	v_cmp_ngt_f32_e64 s[40:41], v20, v4
	s_or_b64 s[40:41], s[38:39], s[40:41]
	s_nop 0
	v_cndmask_b32_e64 v4, v20, v4, s[40:41]
	v_cndmask_b32_e64 v6, 14, v6, s[40:41]
	v_cmp_eq_u32_e64 s[40:41], 15, v2
	v_cmp_ngt_f32_e64 s[42:43], v18, v4
	s_or_b64 s[42:43], s[40:41], s[42:43]
	s_nop 0
	v_cndmask_b32_e64 v4, v18, v4, s[42:43]
	v_cndmask_b32_e64 v6, 15, v6, s[42:43]
	v_cmp_eq_u32_e64 s[42:43], 16, v2
	v_cmp_ngt_f32_e64 s[44:45], v27, v4
	s_or_b64 s[44:45], s[42:43], s[44:45]
	s_nop 0
	v_cndmask_b32_e64 v4, v27, v4, s[44:45]
	v_cndmask_b32_e64 v6, 16, v6, s[44:45]
	v_cmp_eq_u32_e64 s[44:45], 17, v2
	v_cmp_ngt_f32_e64 s[46:47], v25, v4
	s_or_b64 s[46:47], s[44:45], s[46:47]
	s_nop 0
	v_cndmask_b32_e64 v4, v25, v4, s[46:47]
	v_cndmask_b32_e64 v6, 17, v6, s[46:47]
	v_cmp_eq_u32_e64 s[46:47], 18, v2
	v_cmp_ngt_f32_e64 s[48:49], v24, v4
	s_or_b64 s[48:49], s[46:47], s[48:49]
	s_nop 0
	v_cndmask_b32_e64 v4, v24, v4, s[48:49]
	v_cndmask_b32_e64 v6, 18, v6, s[48:49]
	v_cmp_eq_u32_e64 s[48:49], 19, v2
	v_cmp_ngt_f32_e64 s[50:51], v22, v4
	s_or_b64 s[50:51], s[48:49], s[50:51]
	s_nop 0
	v_cndmask_b32_e64 v4, v22, v4, s[50:51]
	v_cndmask_b32_e64 v6, 19, v6, s[50:51]
	v_cmp_eq_u32_e64 s[50:51], 20, v2
	v_cmp_ngt_f32_e64 s[52:53], v31, v4
	s_or_b64 s[52:53], s[50:51], s[52:53]
	s_nop 0
	v_cndmask_b32_e64 v4, v31, v4, s[52:53]
	v_cndmask_b32_e64 v6, 20, v6, s[52:53]
	v_cmp_eq_u32_e64 s[52:53], 21, v2
	v_cmp_ngt_f32_e64 s[54:55], v29, v4
	s_or_b64 s[54:55], s[52:53], s[54:55]
	s_nop 0
	v_cndmask_b32_e64 v4, v29, v4, s[54:55]
	v_cndmask_b32_e64 v6, 21, v6, s[54:55]
	v_cmp_eq_u32_e64 s[54:55], 22, v2
	v_cmp_ngt_f32_e64 s[56:57], v28, v4
	s_or_b64 s[56:57], s[54:55], s[56:57]
	s_nop 0
	v_cndmask_b32_e64 v4, v28, v4, s[56:57]
	v_cndmask_b32_e64 v6, 22, v6, s[56:57]
	v_cmp_eq_u32_e64 s[56:57], 23, v2
	v_cmp_ngt_f32_e64 s[58:59], v26, v4
	s_or_b64 s[58:59], s[56:57], s[58:59]
	s_nop 0
	v_cndmask_b32_e64 v4, v26, v4, s[58:59]
	v_cndmask_b32_e64 v6, 23, v6, s[58:59]
	v_cmp_eq_u32_e64 s[58:59], 24, v2
	v_cmp_ngt_f32_e64 s[60:61], v34, v4
	s_or_b64 s[60:61], s[58:59], s[60:61]
	s_nop 0
	v_cndmask_b32_e64 v4, v34, v4, s[60:61]
; __device__ __forceinline__ void p7_ffn_prep(const Ctx& C, bool dummy = false) {
;     ...
;             for (int k = 0; k < 4; ++k) { float best = -__builtin_inff(); int be = 0;
; #pragma unroll
;                 for (int e = 0; e < 32; ++e) { const bool taken = (k > 0 && e == e4[0]) || (k > 1 && e == e4[1]) || (k > 2 && e == e4[2]); if (!taken && v[e] > best) { best = v[e]; be = e; } }
;                 e4[k] = be; tv[k] = best; }
	v_cndmask_b32_e64 v6, 24, v6, s[60:61]
	v_cmp_eq_u32_e64 s[60:61], 25, v2
	v_cmp_ngt_f32_e64 s[62:63], v33, v4
	s_or_b64 s[62:63], s[60:61], s[62:63]
	s_nop 0
	v_cndmask_b32_e64 v4, v33, v4, s[62:63]
	v_cndmask_b32_e64 v6, 25, v6, s[62:63]
	v_cmp_eq_u32_e64 s[62:63], 26, v2
	v_cmp_ngt_f32_e64 s[64:65], v32, v4
	s_or_b64 s[64:65], s[62:63], s[64:65]
	s_nop 0
	v_cndmask_b32_e64 v4, v32, v4, s[64:65]
	v_cndmask_b32_e64 v6, 26, v6, s[64:65]
	v_cmp_eq_u32_e64 s[64:65], 27, v2
	v_cmp_ngt_f32_e64 s[66:67], v30, v4
	s_or_b64 s[66:67], s[64:65], s[66:67]
	s_nop 0
	v_cndmask_b32_e64 v4, v30, v4, s[66:67]
	v_cndmask_b32_e64 v6, 27, v6, s[66:67]
	v_cmp_eq_u32_e64 s[66:67], 28, v2
	v_cmp_ngt_f32_e64 s[68:69], v35, v4
	s_or_b64 s[68:69], s[66:67], s[68:69]
	s_nop 0
	v_cndmask_b32_e64 v4, v35, v4, s[68:69]
	v_cndmask_b32_e64 v6, 28, v6, s[68:69]
	v_cmp_ngt_f32_e64 s[68:69], v3, v4
	s_or_b64 s[68:69], s[72:73], s[68:69]
	s_nop 0
	v_cndmask_b32_e64 v4, v3, v4, s[68:69]
	v_cndmask_b32_e64 v6, 29, v6, s[68:69]
	v_cmp_ngt_f32_e64 s[68:69], v36, v4
	s_or_b64 s[68:69], s[70:71], s[68:69]
	s_nop 0
	v_cndmask_b32_e64 v4, v36, v4, s[68:69]
	v_cndmask_b32_e64 v6, 30, v6, s[68:69]
	v_cmp_eq_u32_e64 s[68:69], 31, v2
	v_cmp_ngt_f32_e64 s[74:75], v5, v4
	s_or_b64 s[74:75], s[68:69], s[74:75]
	s_nop 0
	v_cndmask_b32_e64 v38, v5, v4, s[74:75]
	v_cndmask_b32_e64 v4, 31, v6, s[74:75]
	v_cmp_eq_u32_e64 s[74:75], 0, v4
	s_or_b64 vcc, vcc, s[74:75]
	v_cndmask_b32_e32 v6, v11, v82, vcc
	v_cmp_eq_u32_e64 s[74:75], 1, v4
	s_or_b64 s[12:13], s[10:11], s[74:75]
	v_cmp_ngt_f32_e64 s[10:11], v9, v6
	s_or_b64 s[10:11], s[12:13], s[10:11]
	s_xor_b64 s[4:5], s[10:11], -1
	v_cndmask_b32_e64 v6, v9, v6, s[10:11]
	v_cmp_eq_u32_e64 s[10:11], 2, v4
	s_or_b64 s[14:15], s[0:1], s[10:11]
	v_cmp_ngt_f32_e64 s[10:11], v8, v6
	v_cndmask_b32_e64 v39, 0, 1, s[4:5]
	s_or_b64 s[10:11], s[14:15], s[10:11]
	v_cndmask_b32_e64 v6, v8, v6, s[10:11]
	v_cndmask_b32_e64 v39, 2, v39, s[10:11]
	v_cmp_eq_u32_e64 s[10:11], 3, v4
	s_or_b64 s[78:79], s[2:3], s[10:11]
	v_cmp_ngt_f32_e64 s[10:11], v7, v6
	s_or_b64 s[10:11], s[78:79], s[10:11]
	s_nop 0
	v_cndmask_b32_e64 v6, v7, v6, s[10:11]
	v_cndmask_b32_e64 v39, 3, v39, s[10:11]
	v_cmp_eq_u32_e64 s[10:11], 4, v4
	s_or_b64 s[76:77], s[16:17], s[10:11]
	v_cmp_ngt_f32_e64 s[10:11], v15, v6
	s_or_b64 s[10:11], s[76:77], s[10:11]
	s_nop 0
	v_cndmask_b32_e64 v6, v15, v6, s[10:11]
	v_cndmask_b32_e64 v39, 4, v39, s[10:11]
	v_cmp_eq_u32_e64 s[10:11], 5, v4
	s_or_b64 s[0:1], s[18:19], s[10:11]
	v_cmp_ngt_f32_e64 s[10:11], v13, v6
	s_or_b64 s[10:11], s[0:1], s[10:11]
	s_xor_b64 s[0:1], s[0:1], -1
	v_cndmask_b32_e64 v6, v13, v6, s[10:11]
	v_cndmask_b32_e64 v39, 5, v39, s[10:11]
	v_cmp_eq_u32_e64 s[10:11], 6, v4
	s_or_b64 s[2:3], s[20:21], s[10:11]
	v_cmp_ngt_f32_e64 s[10:11], v12, v6
	s_or_b64 s[10:11], s[2:3], s[10:11]
	s_nop 0
	v_cndmask_b32_e64 v6, v12, v6, s[10:11]
	v_cndmask_b32_e64 v39, 6, v39, s[10:11]
	v_cmp_eq_u32_e64 s[10:11], 7, v4
	s_or_b64 s[96:97], s[22:23], s[10:11]
	v_cmp_ngt_f32_e64 s[10:11], v10, v6
	s_or_b64 s[10:11], s[96:97], s[10:11]
	s_nop 0
	v_cndmask_b32_e64 v6, v10, v6, s[10:11]
	v_cndmask_b32_e64 v39, 7, v39, s[10:11]
	v_cmp_eq_u32_e64 s[10:11], 8, v4
	s_or_b64 s[94:95], s[24:25], s[10:11]
	v_cmp_ngt_f32_e64 s[10:11], v19, v6
	s_or_b64 s[10:11], s[94:95], s[10:11]
	s_nop 0
	v_cndmask_b32_e64 v6, v19, v6, s[10:11]
	v_cndmask_b32_e64 v39, 8, v39, s[10:11]
	v_cmp_eq_u32_e64 s[10:11], 9, v4
	s_or_b64 s[8:9], s[26:27], s[10:11]
	v_cmp_ngt_f32_e64 s[10:11], v17, v6
	s_or_b64 s[10:11], s[8:9], s[10:11]
	s_nop 0
	v_cndmask_b32_e64 v6, v17, v6, s[10:11]
	v_cndmask_b32_e64 v39, 9, v39, s[10:11]
	v_cmp_eq_u32_e64 s[10:11], 10, v4
	s_or_b64 s[6:7], s[28:29], s[10:11]
	v_cmp_ngt_f32_e64 s[10:11], v16, v6
	s_or_b64 s[10:11], s[6:7], s[10:11]
	s_nop 0
	v_cndmask_b32_e64 v6, v16, v6, s[10:11]
	v_cndmask_b32_e64 v39, 10, v39, s[10:11]
	v_cmp_eq_u32_e64 s[10:11], 11, v4
	s_or_b64 s[80:81], s[30:31], s[10:11]
	v_cmp_ngt_f32_e64 s[10:11], v14, v6
	s_or_b64 s[10:11], s[80:81], s[10:11]
	s_nop 0
	v_cndmask_b32_e64 v6, v14, v6, s[10:11]
	v_cndmask_b32_e64 v39, 11, v39, s[10:11]
	v_cmp_eq_u32_e64 s[10:11], 12, v4
	s_or_b64 s[92:93], s[34:35], s[10:11]
	v_cmp_ngt_f32_e64 s[10:11], v23, v6
	s_or_b64 s[10:11], s[92:93], s[10:11]
	s_nop 0
	v_cndmask_b32_e64 v6, v23, v6, s[10:11]
	v_cndmask_b32_e64 v39, 12, v39, s[10:11]
	v_cmp_eq_u32_e64 s[10:11], 13, v4
	s_or_b64 s[18:19], s[36:37], s[10:11]
	v_cmp_ngt_f32_e64 s[10:11], v21, v6
	s_or_b64 s[10:11], s[18:19], s[10:11]
	s_nop 0
	v_cndmask_b32_e64 v6, v21, v6, s[10:11]
	v_cndmask_b32_e64 v39, 13, v39, s[10:11]
	v_cmp_eq_u32_e64 s[10:11], 14, v4
	s_or_b64 s[4:5], s[38:39], s[10:11]
	v_cmp_ngt_f32_e64 s[10:11], v20, v6
	s_or_b64 s[10:11], s[4:5], s[10:11]
	s_nop 0
	v_cndmask_b32_e64 v6, v20, v6, s[10:11]
	v_cndmask_b32_e64 v39, 14, v39, s[10:11]
	v_cmp_eq_u32_e64 s[10:11], 15, v4
	s_or_b64 s[16:17], s[40:41], s[10:11]
	v_cmp_ngt_f32_e64 s[10:11], v18, v6
	s_or_b64 s[10:11], s[16:17], s[10:11]
	s_nop 0
	v_cndmask_b32_e64 v6, v18, v6, s[10:11]
	v_cndmask_b32_e64 v39, 15, v39, s[10:11]
	v_cmp_eq_u32_e64 s[10:11], 16, v4
	s_or_b64 s[74:75], s[42:43], s[10:11]
	v_cmp_ngt_f32_e64 s[10:11], v27, v6
	s_or_b64 s[10:11], s[74:75], s[10:11]
	s_nop 0
	v_cndmask_b32_e64 v6, v27, v6, s[10:11]
	v_cndmask_b32_e64 v39, 16, v39, s[10:11]
	v_cmp_eq_u32_e64 s[10:11], 17, v4
	s_or_b64 s[42:43], s[44:45], s[10:11]
	v_cmp_ngt_f32_e64 s[10:11], v25, v6
	s_or_b64 s[10:11], s[42:43], s[10:11]
	s_nop 0
	v_cndmask_b32_e64 v6, v25, v6, s[10:11]
	v_cndmask_b32_e64 v39, 17, v39, s[10:11]
	v_cmp_eq_u32_e64 s[10:11], 18, v4
	s_or_b64 s[40:41], s[46:47], s[10:11]
; __device__ __forceinline__ void p7_ffn_prep(const Ctx& C, bool dummy = false) {
;     ...
;             for (int k = 0; k < 4; ++k) { float best = -__builtin_inff(); int be = 0;
; #pragma unroll
;                 for (int e = 0; e < 32; ++e) { const bool taken = (k > 0 && e == e4[0]) || (k > 1 && e == e4[1]) || (k > 2 && e == e4[2]); if (!taken && v[e] > best) { best = v[e]; be = e; } }
;                 e4[k] = be; tv[k] = best; }
	v_cmp_ngt_f32_e64 s[10:11], v24, v6
	s_or_b64 s[10:11], s[40:41], s[10:11]
	s_nop 0
	v_cndmask_b32_e64 v6, v24, v6, s[10:11]
	v_cndmask_b32_e64 v39, 18, v39, s[10:11]
	v_cmp_eq_u32_e64 s[10:11], 19, v4
	s_or_b64 s[38:39], s[48:49], s[10:11]
	v_cmp_ngt_f32_e64 s[10:11], v22, v6
	s_or_b64 s[10:11], s[38:39], s[10:11]
	s_nop 0
	v_cndmask_b32_e64 v6, v22, v6, s[10:11]
	v_cndmask_b32_e64 v39, 19, v39, s[10:11]
	v_cmp_eq_u32_e64 s[10:11], 20, v4
	s_or_b64 s[36:37], s[50:51], s[10:11]
	v_cmp_ngt_f32_e64 s[10:11], v31, v6
	s_or_b64 s[10:11], s[36:37], s[10:11]
	s_nop 0
	v_cndmask_b32_e64 v6, v31, v6, s[10:11]
	v_cndmask_b32_e64 v39, 20, v39, s[10:11]
	v_cmp_eq_u32_e64 s[10:11], 21, v4
	s_or_b64 s[34:35], s[52:53], s[10:11]
	v_cmp_ngt_f32_e64 s[10:11], v29, v6
	s_or_b64 s[10:11], s[34:35], s[10:11]
	s_nop 0
	v_cndmask_b32_e64 v6, v29, v6, s[10:11]
	v_cndmask_b32_e64 v39, 21, v39, s[10:11]
	v_cmp_eq_u32_e64 s[10:11], 22, v4
	s_or_b64 s[30:31], s[54:55], s[10:11]
	v_cmp_ngt_f32_e64 s[10:11], v28, v6
	s_or_b64 s[10:11], s[30:31], s[10:11]
	s_nop 0
	v_cndmask_b32_e64 v6, v28, v6, s[10:11]
	v_cndmask_b32_e64 v39, 22, v39, s[10:11]
	v_cmp_eq_u32_e64 s[10:11], 23, v4
	s_or_b64 s[28:29], s[56:57], s[10:11]
	v_cmp_ngt_f32_e64 s[10:11], v26, v6
	s_or_b64 s[10:11], s[28:29], s[10:11]
	s_nop 0
	v_cndmask_b32_e64 v6, v26, v6, s[10:11]
	v_cndmask_b32_e64 v39, 23, v39, s[10:11]
	v_cmp_eq_u32_e64 s[10:11], 24, v4
	s_or_b64 s[26:27], s[58:59], s[10:11]
	v_cmp_ngt_f32_e64 s[10:11], v34, v6
	s_or_b64 s[10:11], s[26:27], s[10:11]
	s_nop 0
	v_cndmask_b32_e64 v6, v34, v6, s[10:11]
	v_cndmask_b32_e64 v39, 24, v39, s[10:11]
	v_cmp_eq_u32_e64 s[10:11], 25, v4
	s_or_b64 s[24:25], s[60:61], s[10:11]
	v_cmp_ngt_f32_e64 s[10:11], v33, v6
	s_or_b64 s[10:11], s[24:25], s[10:11]
	s_nop 0
	v_cndmask_b32_e64 v6, v33, v6, s[10:11]
	v_cndmask_b32_e64 v39, 25, v39, s[10:11]
	v_cmp_eq_u32_e64 s[10:11], 26, v4
	s_or_b64 s[22:23], s[62:63], s[10:11]
	v_cmp_ngt_f32_e64 s[10:11], v32, v6
	s_or_b64 s[10:11], s[22:23], s[10:11]
	v_readlane_b32 s60, v254, 8
	v_cndmask_b32_e64 v6, v32, v6, s[10:11]
	v_cndmask_b32_e64 v39, 26, v39, s[10:11]
	v_cmp_eq_u32_e64 s[10:11], 27, v4
	s_or_b64 s[20:21], s[64:65], s[10:11]
	v_cmp_ngt_f32_e64 s[10:11], v30, v6
	s_or_b64 s[10:11], s[20:21], s[10:11]
	v_readlane_b32 s61, v254, 9
	v_cndmask_b32_e64 v6, v30, v6, s[10:11]
	v_cndmask_b32_e64 v39, 27, v39, s[10:11]
	v_cmp_eq_u32_e64 s[10:11], 28, v4
	s_or_b64 s[50:51], s[66:67], s[10:11]
	v_cmp_ngt_f32_e64 s[10:11], v35, v6
	s_or_b64 s[10:11], s[50:51], s[10:11]
	v_readlane_b32 s62, v254, 10
	v_cndmask_b32_e64 v6, v35, v6, s[10:11]
	v_cndmask_b32_e64 v39, 28, v39, s[10:11]
	v_cmp_eq_u32_e64 s[10:11], 29, v4
	s_or_b64 s[48:49], s[72:73], s[10:11]
	v_cmp_ngt_f32_e64 s[10:11], v3, v6
	s_or_b64 s[10:11], s[48:49], s[10:11]
	v_readlane_b32 s63, v254, 11
	v_cndmask_b32_e64 v6, v3, v6, s[10:11]
	v_cndmask_b32_e64 v39, 29, v39, s[10:11]
	v_cmp_eq_u32_e64 s[10:11], 30, v4
	s_or_b64 s[46:47], s[70:71], s[10:11]
	v_cmp_ngt_f32_e64 s[10:11], v36, v6
	s_or_b64 s[10:11], s[46:47], s[10:11]
	s_nop 0
	v_cndmask_b32_e64 v6, v36, v6, s[10:11]
	v_cndmask_b32_e64 v39, 30, v39, s[10:11]
	v_cmp_eq_u32_e64 s[10:11], 31, v4
	s_or_b64 s[44:45], s[68:69], s[10:11]
	v_cmp_ngt_f32_e64 s[10:11], v5, v6
	s_or_b64 s[10:11], s[44:45], s[10:11]
	s_nop 0
	v_cndmask_b32_e64 v40, v5, v6, s[10:11]
	v_cndmask_b32_e64 v6, 31, v39, s[10:11]
	v_cmp_eq_u32_e64 s[10:11], 0, v6
	s_or_b64 vcc, vcc, s[10:11]
	v_cndmask_b32_e32 v11, v11, v82, vcc
	v_cmp_ne_u32_e32 vcc, 1, v6
	s_xor_b64 s[10:11], s[12:13], -1
	s_and_b64 s[10:11], s[10:11], vcc
	v_cmp_gt_f32_e32 vcc, v9, v11
	s_and_b64 vcc, s[10:11], vcc
	s_xor_b64 s[10:11], s[14:15], -1
	v_cndmask_b32_e32 v9, v11, v9, vcc
	v_cndmask_b32_e64 v11, 0, 1, vcc
	v_cmp_ne_u32_e32 vcc, 2, v6
	s_and_b64 s[10:11], s[10:11], vcc
	v_cmp_gt_f32_e32 vcc, v8, v9
	s_and_b64 vcc, s[10:11], vcc
	s_xor_b64 s[10:11], s[78:79], -1
	v_cndmask_b32_e32 v8, v9, v8, vcc
	v_cndmask_b32_e64 v9, v11, 2, vcc
	v_cmp_ne_u32_e32 vcc, 3, v6
	s_and_b64 s[10:11], s[10:11], vcc
	v_cmp_gt_f32_e32 vcc, v7, v8
	s_and_b64 vcc, s[10:11], vcc
	s_xor_b64 s[10:11], s[76:77], -1
	v_cndmask_b32_e32 v7, v8, v7, vcc
	v_cndmask_b32_e64 v8, v9, 3, vcc
	v_cmp_ne_u32_e32 vcc, 4, v6
	s_and_b64 s[10:11], s[10:11], vcc
	v_cmp_gt_f32_e32 vcc, v15, v7
	s_and_b64 vcc, s[10:11], vcc
	s_nop 0
	v_cndmask_b32_e32 v7, v7, v15, vcc
	v_cndmask_b32_e64 v8, v8, 4, vcc
	v_cmp_ne_u32_e32 vcc, 5, v6
	s_and_b64 s[0:1], s[0:1], vcc
	v_cmp_gt_f32_e32 vcc, v13, v7
	s_and_b64 vcc, s[0:1], vcc
	s_xor_b64 s[0:1], s[2:3], -1
	v_cndmask_b32_e32 v7, v7, v13, vcc
	v_cndmask_b32_e64 v8, v8, 5, vcc
	v_cmp_ne_u32_e32 vcc, 6, v6
	s_and_b64 s[0:1], s[0:1], vcc
	v_cmp_gt_f32_e32 vcc, v12, v7
	s_and_b64 vcc, s[0:1], vcc
	s_xor_b64 s[0:1], s[96:97], -1
	v_cndmask_b32_e32 v7, v7, v12, vcc
	v_cndmask_b32_e64 v8, v8, 6, vcc
	v_cmp_ne_u32_e32 vcc, 7, v6
	s_and_b64 s[0:1], s[0:1], vcc
	v_cmp_gt_f32_e32 vcc, v10, v7
	s_and_b64 vcc, s[0:1], vcc
	s_xor_b64 s[0:1], s[94:95], -1
	v_cndmask_b32_e32 v7, v7, v10, vcc
	v_cndmask_b32_e64 v8, v8, 7, vcc
	v_cmp_ne_u32_e32 vcc, 8, v6
	s_and_b64 s[0:1], s[0:1], vcc
	v_cmp_gt_f32_e32 vcc, v19, v7
	s_and_b64 vcc, s[0:1], vcc
	s_xor_b64 s[0:1], s[8:9], -1
	v_cndmask_b32_e32 v7, v7, v19, vcc
	v_cndmask_b32_e64 v8, v8, 8, vcc
	v_cmp_ne_u32_e32 vcc, 9, v6
	s_and_b64 s[0:1], s[0:1], vcc
	v_cmp_gt_f32_e32 vcc, v17, v7
	s_and_b64 vcc, s[0:1], vcc
	s_xor_b64 s[0:1], s[6:7], -1
	v_cndmask_b32_e32 v7, v7, v17, vcc
	v_cndmask_b32_e64 v8, v8, 9, vcc
	v_cmp_ne_u32_e32 vcc, 10, v6
	s_and_b64 s[0:1], s[0:1], vcc
	v_cmp_gt_f32_e32 vcc, v16, v7
	s_and_b64 vcc, s[0:1], vcc
; __device__ __forceinline__ void p7_ffn_prep(const Ctx& C, bool dummy = false) {
;     ...
;             for (int k = 0; k < 4; ++k) { float best = -__builtin_inff(); int be = 0;
; #pragma unroll
;                 for (int e = 0; e < 32; ++e) { const bool taken = (k > 0 && e == e4[0]) || (k > 1 && e == e4[1]) || (k > 2 && e == e4[2]); if (!taken && v[e] > best) { best = v[e]; be = e; } }
;                 e4[k] = be; tv[k] = best; }
;             const float p1 = __expf(tv[1] - tv[0]), p2 = __expf(tv[2] - tv[0]), p3 = __expf(tv[3] - tv[0]); const float inv = 1.0f / (1.0f + p1 + p2 + p3);
;             gk[0] = inv; gk[1] = p1 * inv; gk[2] = p2 * inv; gk[3] = p3 * inv;
; #pragma unroll
;             for (int k = 0; k < 4; ++k) rk[k] = __hip_atomic_fetch_add(cnt + e4[k], 1, __ATOMIC_RELAXED, __HIP_MEMORY_SCOPE_WORKGROUP);
	s_xor_b64 s[0:1], s[80:81], -1
	v_cndmask_b32_e32 v7, v7, v16, vcc
	v_cndmask_b32_e64 v8, v8, 10, vcc
	v_cmp_ne_u32_e32 vcc, 11, v6
	s_and_b64 s[0:1], s[0:1], vcc
	v_cmp_gt_f32_e32 vcc, v14, v7
	s_and_b64 vcc, s[0:1], vcc
	s_xor_b64 s[0:1], s[92:93], -1
	v_cndmask_b32_e32 v7, v7, v14, vcc
	v_cndmask_b32_e64 v8, v8, 11, vcc
	v_cmp_ne_u32_e32 vcc, 12, v6
	s_and_b64 s[0:1], s[0:1], vcc
	v_cmp_gt_f32_e32 vcc, v23, v7
	s_and_b64 vcc, s[0:1], vcc
	s_xor_b64 s[0:1], s[18:19], -1
	v_cndmask_b32_e32 v7, v7, v23, vcc
	v_cndmask_b32_e64 v8, v8, 12, vcc
	v_cmp_ne_u32_e32 vcc, 13, v6
	s_and_b64 s[0:1], s[0:1], vcc
	v_cmp_gt_f32_e32 vcc, v21, v7
	s_and_b64 vcc, s[0:1], vcc
	s_xor_b64 s[0:1], s[4:5], -1
	v_cndmask_b32_e32 v7, v7, v21, vcc
	v_cndmask_b32_e64 v8, v8, 13, vcc
	v_cmp_ne_u32_e32 vcc, 14, v6
	s_and_b64 s[0:1], s[0:1], vcc
	v_cmp_gt_f32_e32 vcc, v20, v7
	s_and_b64 vcc, s[0:1], vcc
	s_xor_b64 s[0:1], s[16:17], -1
	v_cndmask_b32_e32 v7, v7, v20, vcc
	v_cndmask_b32_e64 v8, v8, 14, vcc
	v_cmp_ne_u32_e32 vcc, 15, v6
	s_and_b64 s[0:1], s[0:1], vcc
	v_cmp_gt_f32_e32 vcc, v18, v7
	s_and_b64 vcc, s[0:1], vcc
	s_xor_b64 s[0:1], s[74:75], -1
	v_cndmask_b32_e32 v7, v7, v18, vcc
	v_cndmask_b32_e64 v8, v8, 15, vcc
	v_cmp_ne_u32_e32 vcc, 16, v6
	s_and_b64 s[0:1], s[0:1], vcc
	v_cmp_gt_f32_e32 vcc, v27, v7
	s_and_b64 vcc, s[0:1], vcc
	s_xor_b64 s[0:1], s[42:43], -1
	v_cndmask_b32_e32 v7, v7, v27, vcc
	v_cndmask_b32_e64 v8, v8, 16, vcc
	v_cmp_ne_u32_e32 vcc, 17, v6
	s_and_b64 s[0:1], s[0:1], vcc
	v_cmp_gt_f32_e32 vcc, v25, v7
	s_and_b64 vcc, s[0:1], vcc
	s_xor_b64 s[0:1], s[40:41], -1
	v_cndmask_b32_e32 v7, v7, v25, vcc
	v_cndmask_b32_e64 v8, v8, 17, vcc
	v_cmp_ne_u32_e32 vcc, 18, v6
	s_and_b64 s[0:1], s[0:1], vcc
	v_cmp_gt_f32_e32 vcc, v24, v7
	s_and_b64 vcc, s[0:1], vcc
	s_xor_b64 s[0:1], s[38:39], -1
	v_cndmask_b32_e32 v7, v7, v24, vcc
	v_cndmask_b32_e64 v8, v8, 18, vcc
	v_cmp_ne_u32_e32 vcc, 19, v6
	s_and_b64 s[0:1], s[0:1], vcc
	v_cmp_gt_f32_e32 vcc, v22, v7
	s_and_b64 vcc, s[0:1], vcc
	s_xor_b64 s[0:1], s[36:37], -1
	v_cndmask_b32_e32 v7, v7, v22, vcc
	v_cndmask_b32_e64 v8, v8, 19, vcc
	v_cmp_ne_u32_e32 vcc, 20, v6
	s_and_b64 s[0:1], s[0:1], vcc
	v_cmp_gt_f32_e32 vcc, v31, v7
	s_and_b64 vcc, s[0:1], vcc
	s_xor_b64 s[0:1], s[34:35], -1
	v_cndmask_b32_e32 v7, v7, v31, vcc
	v_cndmask_b32_e64 v8, v8, 20, vcc
	v_cmp_ne_u32_e32 vcc, 21, v6
	s_and_b64 s[0:1], s[0:1], vcc
	v_cmp_gt_f32_e32 vcc, v29, v7
	s_and_b64 vcc, s[0:1], vcc
	s_xor_b64 s[0:1], s[30:31], -1
	v_cndmask_b32_e32 v7, v7, v29, vcc
	v_cndmask_b32_e64 v8, v8, 21, vcc
	v_cmp_ne_u32_e32 vcc, 22, v6
	s_and_b64 s[0:1], s[0:1], vcc
	v_cmp_gt_f32_e32 vcc, v28, v7
	s_and_b64 vcc, s[0:1], vcc
	s_xor_b64 s[0:1], s[28:29], -1
	v_cndmask_b32_e32 v7, v7, v28, vcc
	v_cndmask_b32_e64 v8, v8, 22, vcc
	v_cmp_ne_u32_e32 vcc, 23, v6
	s_and_b64 s[0:1], s[0:1], vcc
	v_cmp_gt_f32_e32 vcc, v26, v7
	s_and_b64 vcc, s[0:1], vcc
	s_xor_b64 s[0:1], s[26:27], -1
	v_cndmask_b32_e32 v7, v7, v26, vcc
	v_cndmask_b32_e64 v8, v8, 23, vcc
	v_cmp_ne_u32_e32 vcc, 24, v6
	s_and_b64 s[0:1], s[0:1], vcc
	v_cmp_gt_f32_e32 vcc, v34, v7
	s_and_b64 vcc, s[0:1], vcc
	s_xor_b64 s[0:1], s[24:25], -1
	v_cndmask_b32_e32 v7, v7, v34, vcc
	v_cndmask_b32_e64 v8, v8, 24, vcc
	v_cmp_ne_u32_e32 vcc, 25, v6
	s_and_b64 s[0:1], s[0:1], vcc
	v_cmp_gt_f32_e32 vcc, v33, v7
	s_and_b64 vcc, s[0:1], vcc
	s_xor_b64 s[0:1], s[22:23], -1
	v_cndmask_b32_e32 v7, v7, v33, vcc
	v_cndmask_b32_e64 v8, v8, 25, vcc
	v_cmp_ne_u32_e32 vcc, 26, v6
	s_and_b64 s[0:1], s[0:1], vcc
	v_cmp_gt_f32_e32 vcc, v32, v7
	s_and_b64 vcc, s[0:1], vcc
	s_xor_b64 s[0:1], s[20:21], -1
	v_cndmask_b32_e32 v7, v7, v32, vcc
	v_cndmask_b32_e64 v8, v8, 26, vcc
	v_cmp_ne_u32_e32 vcc, 27, v6
	s_and_b64 s[0:1], s[0:1], vcc
	v_cmp_gt_f32_e32 vcc, v30, v7
	s_and_b64 vcc, s[0:1], vcc
	s_xor_b64 s[0:1], s[50:51], -1
	v_cndmask_b32_e32 v7, v7, v30, vcc
	v_cndmask_b32_e64 v8, v8, 27, vcc
	v_cmp_ne_u32_e32 vcc, 28, v6
	s_and_b64 s[0:1], s[0:1], vcc
	v_cmp_gt_f32_e32 vcc, v35, v7
	s_and_b64 vcc, s[0:1], vcc
	s_xor_b64 s[0:1], s[48:49], -1
	v_cndmask_b32_e32 v7, v7, v35, vcc
	v_cndmask_b32_e64 v8, v8, 28, vcc
	v_cmp_ne_u32_e32 vcc, 29, v6
	s_and_b64 s[0:1], s[0:1], vcc
	v_cmp_gt_f32_e32 vcc, v3, v7
	s_and_b64 vcc, s[0:1], vcc
	s_xor_b64 s[0:1], s[46:47], -1
	v_cndmask_b32_e32 v3, v7, v3, vcc
	v_cndmask_b32_e64 v7, v8, 29, vcc
	v_cmp_ne_u32_e32 vcc, 30, v6
	s_and_b64 s[0:1], s[0:1], vcc
	v_cmp_gt_f32_e32 vcc, v36, v3
	s_and_b64 vcc, s[0:1], vcc
	s_xor_b64 s[0:1], s[44:45], -1
	v_cndmask_b32_e32 v3, v3, v36, vcc
	v_cndmask_b32_e64 v7, v7, 30, vcc
	v_cmp_ne_u32_e32 vcc, 31, v6
	s_and_b64 s[0:1], s[0:1], vcc
	v_cmp_gt_f32_e32 vcc, v5, v3
	s_and_b64 vcc, s[0:1], vcc
	s_nop 0
	v_cndmask_b32_e32 v3, v3, v5, vcc
	v_sub_f32_e32 v5, v38, v37
	v_mul_f32_e32 v5, 0x3fb8aa3b, v5
	v_exp_f32_e32 v10, v5
	v_sub_f32_e32 v5, v40, v37
	v_mul_f32_e32 v5, 0x3fb8aa3b, v5
	v_sub_f32_e32 v3, v3, v37
	v_exp_f32_e32 v11, v5
	v_mul_f32_e32 v3, 0x3fb8aa3b, v3
	v_exp_f32_e32 v3, v3
	v_add_f32_e32 v5, 1.0, v10
	v_add_f32_e32 v5, v5, v11
	v_cndmask_b32_e64 v8, v7, 31, vcc
	v_add_f32_e32 v5, v5, v3
	v_div_scale_f32 v7, s[0:1], v5, v5, 1.0
	v_rcp_f32_e32 v9, v7
	s_nop 0
	v_fma_f32 v12, -v7, v9, 1.0
	v_fmac_f32_e32 v9, v12, v9
	v_div_scale_f32 v12, vcc, 1.0, v5, 1.0
	v_mul_f32_e32 v13, v12, v9
	v_fma_f32 v14, -v7, v13, v12
	v_fmac_f32_e32 v13, v14, v9
	v_fma_f32 v7, -v7, v13, v12
	v_div_fmas_f32 v7, v7, v9, v13
	v_div_fixup_f32 v12, v7, v5, 1.0
	v_pk_mul_f32 v[10:11], v[10:11], v[12:13] op_sel_hi:[1,0]
	v_mul_f32_e32 v13, v3, v12
	v_lshl_add_u32 v3, v2, 2, 0
	ds_add_rtn_u32 v20, v3, v80
	v_lshl_add_u32 v3, v4, 2, 0
	ds_add_rtn_u32 v18, v3, v80
	v_lshl_add_u32 v3, v6, 2, 0
	ds_add_rtn_u32 v16, v3, v80
	v_lshl_add_u32 v3, v8, 2, 0
	ds_add_rtn_u32 v14, v3, v80
